# phase reorder: workgroup groups 4-7 defer their expert-weight f32->bf16 conversion from P1 to after router0 (before the grid barrier), so memory-bound conversion overlaps the other groups GEMM phases;
# speedup vs baseline: 1.0236x; 1.0169x over previous
; #define LAS __attribute__((address_space(3)))
; #define KIN(i) ((const float*)(GAS const float*)karg()[i])
; #define WSP(type, off) ((type*)(KWS() + (off)))
; #define IDS() const int lane = lane_id(), tid = wave * 64 + lane; (void)tid; (void)lane
; __global__ void __launch_bounds__(NWAVES * 64, 2) mk_fwd(Args args) {
;     ...
;     for (int rep_ = 0; rep_ < REPS(1); ++rep_) if (IN(1)) { IDS();
;         {
;         LAS float* scr = (LAS float*)(lds + wave * 16640);
;         const float* conv_in_w = KIN(6); const float* conv_out_w = KIN(8); const float* attn_in_w = KIN(9); const float* attn_out_w = KIN(10);
;         const float* gate_w = KIN(15); const float* up_w = KIN(16); const float* down_w = KIN(17);
;         bf16_t* WZ = WSP(bf16_t, WS_WZ); bf16_t* WB = WSP(bf16_t, WS_WB); bf16_t* WCO = WSP(bf16_t, WS_WCO); bf16_t* WAI = WSP(bf16_t, WS_WAI); bf16_t* WAO = WSP(bf16_t, WS_WAO);
;         bf16_t* WGU = WSP(bf16_t, WS_WGU); bf16_t* WDN = WSP(bf16_t, WS_WDN);
;     ...
;         {
;             const int step = G * NWAVES; int it0 = CONV_EARLY + bid * NWAVES + wave;
;             ConvDesc dA, dB; f32x4 vA[16], vB[16];
;             if (it0 < NCONV_ITEMS) { CONV_DECODE(dA, it0); conv_load(vA, dA, lane); }
; #pragma unroll 1
;             for (; it0 < NCONV_ITEMS; it0 += 2 * step) {
;                 const bool hasB = it0 + step < NCONV_ITEMS, hasA2 = it0 + 2 * step < NCONV_ITEMS;
;                 if (hasB) { CONV_DECODE(dB, it0 + step); conv_load(vB, dB, lane); }
.LBB0_399:
	s_or_b64 exec, exec, s[0:1]
	s_mov_b64 s[0:1], s[78:79]
	s_waitcnt lgkmcnt(0)
	s_barrier
	s_mov_b32 s99, 0
.Lconv_entry:
	s_bitcmp1_b32 s83, 2
	s_cbranch_scc0 .Lconv_go
	s_cmp_eq_u32 s99, 0
	s_cbranch_scc0 .Lconv_go
	v_mbcnt_lo_u32_b32 v64, -1, 0
	v_mbcnt_hi_u32_b32 v64, -1, v64
	s_lshl_b32 s50, s83, 5
	v_lshlrev_b32_e32 v132, 2, v64
	s_branch .LBB0_739
.Lconv_go:
	v_mbcnt_lo_u32_b32 v64, -1, 0
	v_mbcnt_hi_u32_b32 v64, -1, v64
	s_load_dwordx2 s[8:9], s[0:1], 0x30
	s_mov_b64 s[0:1], s[78:79]
	s_load_dwordx2 s[10:11], s[0:1], 0x40
	s_mov_b64 s[0:1], s[78:79]
	s_load_dwordx2 s[12:13], s[0:1], 0x48
	s_mov_b64 s[0:1], s[78:79]
	s_load_dwordx2 s[14:15], s[0:1], 0x50
	s_mov_b64 s[0:1], s[78:79]
	s_load_dwordx2 s[16:17], s[0:1], 0x78
	s_mov_b64 s[0:1], s[78:79]
	s_load_dwordx2 s[18:19], s[0:1], 0x80
	s_mov_b64 s[0:1], s[78:79]
	s_load_dwordx2 s[20:21], s[0:1], 0x88
	s_mov_b64 s[0:1], s[78:79]
	s_load_dwordx2 s[22:23], s[0:1], 0xa0
	s_mov_b64 s[24:25], s[78:79]
	s_mov_b64 s[26:27], s[78:79]
	v_mov_b32_e32 v0, 0x900
	v_add_co_u32_e64 v0, s[6:7], s50, v0
	s_waitcnt lgkmcnt(0)
	s_add_u32 s38, s22, 0x2000000
	s_addc_u32 s39, s23, 0
	s_mov_b64 s[22:23], s[78:79]
	s_load_dwordx2 s[22:23], s[22:23], 0xa0
	s_load_dwordx2 s[24:25], s[24:25], 0xa0
	s_load_dwordx2 s[26:27], s[26:27], 0xa0
	s_waitcnt lgkmcnt(0)
	s_add_u32 s40, s22, 0x2400000
	s_addc_u32 s41, s23, 0
	s_mov_b64 s[22:23], s[78:79]
	s_add_u32 s42, s24, 0x2600000
	s_addc_u32 s43, s25, 0
	s_load_dwordx2 s[22:23], s[22:23], 0xa0
	s_mov_b64 s[24:25], s[78:79]
	s_add_u32 s44, s26, 0x2800000
	s_addc_u32 s45, s27, 0
	s_load_dwordx2 s[24:25], s[24:25], 0xa0
	s_mov_b64 s[26:27], s[78:79]
	s_load_dwordx2 s[26:27], s[26:27], 0xa0
	s_waitcnt lgkmcnt(0)
	s_add_u32 s46, s22, 0x3100000
	s_addc_u32 s47, s23, 0
	s_add_u32 s51, s24, 0x4000000
	s_movk_i32 s0, 0x6900
	s_addc_u32 s52, s25, 0
	v_cmp_gt_i32_e64 s[0:1], s0, v0
	s_add_u32 s53, s26, 0xc000000
	v_readfirstlane_b32 s69, v0
	s_addc_u32 s54, s27, 0
	s_and_b64 vcc, exec, s[0:1]
	s_cbranch_vccz .LBB0_408
	s_cmpk_gt_i32 s69, 0x1ff
	s_cbranch_scc0 .LBB0_409
	s_lshl_b32 s55, s69, 2
	s_lshl_b32 s22, s69, 6
	s_and_b32 s36, s22, 0x3c0
	s_and_b32 s37, s55, 0xfc0
	s_cmpk_gt_u32 s69, 0x2ff
	s_cbranch_scc0 .LBB0_410
	s_cmpk_gt_u32 s69, 0x3ff
	s_cbranch_scc0 .LBB0_411
	s_cmpk_gt_u32 s69, 0x87f
	s_cbranch_scc0 .LBB0_412
	s_andn2_b64 vcc, exec, s[6:7]
	s_cbranch_vccz .LBB0_413
	s_mul_hi_u32 s6, s50, 0xaaaaaaab
	s_lshr_b32 s6, s6, 8
	s_mul_i32 s7, s6, 0x180
	s_sub_i32 s23, s50, s7
	s_mov_b32 s7, 0
	s_lshl_b32 s22, s23, 6
	s_lshl_b64 s[30:31], s[6:7], 21
	s_lshl_b32 s56, s23, 3
	s_and_b32 s50, s22, 0x1c0
	s_cmpk_gt_u32 s23, 0x7f
	s_cbranch_scc0 .LBB0_414
	s_cmpk_gt_u32 s23, 0xff
	s_cbranch_scc0 .LBB0_415
	s_lshl_b64 s[24:25], s[6:7], 20
	s_lshl_b32 s6, s23, 2
	s_and_b32 s6, s6, 0x7c0
	s_add_i32 s28, s6, 0xfffffc00
	s_mov_b32 s29, 0
	s_lshl_b64 s[26:27], s[28:29], 12
	s_and_b32 s6, s22, 0x3c0
	s_add_u32 s7, s20, s30
	s_addc_u32 s22, s21, s31
	s_add_u32 s24, s53, s24
	s_addc_u32 s25, s54, s25
	s_add_u32 s7, s7, s26
	s_addc_u32 s22, s22, s27
	s_lshl_b32 s23, s6, 2
	s_add_u32 s26, s7, s23
	s_addc_u32 s27, s22, 0
	s_lshl_b64 s[22:23], s[28:29], 1
	s_add_u32 s24, s24, s22
	s_addc_u32 s25, s25, s23
	s_mov_b64 s[22:23], 0
	s_branch .LBB0_416

; #define KIN(i) ((const float*)(GAS const float*)karg()[i])
; #define WSP(type, off) ((type*)(KWS() + (off)))
; #define CBID() (LOCAL_OK() ? ((bid & 7) * 32 + (bid >> 3)) : bid)
; __global__ void __launch_bounds__(NWAVES * 64, 2) mk_fwd(Args args) {
;     ...
;         const float* x = KIN(0); const float* norm_mix_g = KIN(2); const float* mod = WSP(float, WS_MOD); bf16_t* xn = WSP(bf16_t, WS_XN);
;         for (int w0 = (CBID() * 8 + wave) * 32; w0 < T; w0 += G * 8 * 32) {
;             const float* mb = mod + (size_t)(w0 >> 12) * 6144;
;             ModV mv; mod_load(mv, norm_mix_g, mb + 0, mb + 1024, lane);
;             RowV ring[4];
; #pragma unroll
;             for (int d = 0; d < 4; ++d) row_load(ring[d], x + (size_t)(w0 + d) * D, lane);
.LBB0_739:
	s_cmp_eq_u32 s99, 1
	s_cbranch_scc1 .Lseam5_go
	s_cmpk_lg_i32 s33, 0x100
	s_cselect_b64 s[0:1], -1, 0
	v_writelane_b32 v251, s0, 9
	s_and_b32 s54, s50, 0xe0
	s_mov_b64 s[8:9], s[78:79]
	v_writelane_b32 v251, s1, 10
	s_lshr_b32 s0, s83, 3
	s_add_i32 s6, s54, s0
	s_cmpk_eq_i32 s33, 0x100
	s_cselect_b64 s[2:3], -1, 0
	s_and_b64 s[0:1], s[2:3], exec
	s_cselect_b32 s0, s6, s83
	s_lshl_b32 s0, s0, 8
	s_lshl_b32 s96, s85, 5
	s_add_i32 s6, s0, s96
	s_lshl_b32 s0, s33, 8
	v_writelane_b32 v251, s0, 11
	s_cmp_gt_i32 s6, 0xffff
	s_mov_b64 s[10:11], s[78:79]
	v_writelane_b32 v251, s1, 12
	s_mov_b64 s[0:1], s[78:79]
	s_mov_b64 s[12:13], s[78:79]
	s_cbranch_scc1 .LBB0_754
	s_load_dwordx2 s[14:15], s[10:11], 0xa0
	s_load_dwordx2 s[16:17], s[0:1], 0x0
	s_load_dwordx2 s[20:21], s[8:9], 0x10
	s_load_dwordx2 s[22:23], s[12:13], 0xa0
	v_ashrrev_i32_e32 v133, 31, v132
	s_waitcnt vmcnt(15)
	v_lshlrev_b64 v[0:1], 2, v[132:133]
	s_waitcnt lgkmcnt(0)
	s_add_u32 s18, s14, 0x100000
	v_lshl_add_u64 v[96:97], s[20:21], 0, v[0:1]
	v_lshl_add_u64 v[98:99], s[16:17], 0, v[0:1]
	v_lshlrev_b64 v[0:1], 1, v[132:133]
	s_addc_u32 s19, s15, 0
	v_lshl_add_u64 v[2:3], s[22:23], 0, v[0:1]
	s_mov_b64 s[0:1], 0x10000000
	s_ashr_i32 s7, s6, 31
	v_lshl_add_u64 v[100:101], v[2:3], 0, s[0:1]
	s_lshl_b64 s[0:1], s[6:7], 11
	s_add_u32 s0, s22, s0
	s_addc_u32 s1, s23, s1
	v_lshl_add_u64 v[0:1], s[0:1], 0, v[0:1]
	s_mov_b64 s[0:1], 0x10000400
	v_lshl_add_u64 v[102:103], v[0:1], 0, s[0:1]
	v_readlane_b32 s0, v251, 11
	v_readlane_b32 s1, v251, 12
	s_mov_b32 s8, s0
	s_ashr_i32 s9, s0, 31
	v_writelane_b32 v251, s0, 11
	s_lshl_b64 s[8:9], s[8:9], 11
	s_mov_b64 s[10:11], 0x1000
	v_mov_b32_e32 v122, 0x358637bd
	s_mov_b64 s[12:13], 0x2000
	v_writelane_b32 v251, s1, 12
	s_branch .LBB0_742

; #define KIN(i) ((const float*)(GAS const float*)karg()[i])
; #define KOUT() ((float*)(GAS float*)karg()[19])
; #define KWS() ((unsigned char*)(GAS unsigned char*)karg()[20])
; #define WSP(type, off) ((type*)(KWS() + (off)))
; #define CBID() (LOCAL_OK() ? ((bid & 7) * 32 + (bid >> 3)) : bid)
; #define SEAM(k) do { if (IN(k) && IN((k) + 1)) GRID_BAR(); } while (0)
; #define MODL() (WSP(float, WS_MOD) + (size_t)l * 16 * 6144)
; #define CNTL() (WSP(int, WS_CTL) + 64 * l)
; #define MODL() (WSP(float, WS_MOD) + (size_t)l * 16 * 6144)
; #define CNTL() (WSP(int, WS_CTL) + 64 * l)
; __global__ void __launch_bounds__(NWAVES * 64, 2) mk_fwd(Args args) {
;     ...
;         {
;             const int step = G * NWAVES; int it0 = CONV_EARLY + bid * NWAVES + wave;
;             ConvDesc dA, dB; f32x4 vA[16], vB[16];
;             if (it0 < NCONV_ITEMS) { CONV_DECODE(dA, it0); conv_load(vA, dA, lane); }
;     ...
;         if (IN(pb0)) rt::router_phase(lds, (const bf16_t*)KOUT(), WSP(bf16_t, WS_XN), KIN(3) + l * D, MODL(), KIN(11) + (size_t)l * D * 4, KIN(12) + l * 4, KIN(13) + (size_t)l * 4 * D * 8, KIN(14) + l * 32,
;                                       CNTL(), WSP(int, WS_LTOK), WSP(float, WS_LW), WSP(int, WS_TSLOT), CBID(), G, wave, LOCAL_OK() ? (const unsigned char*)(KWS() + WS_RTAB + (size_t)l * 16 * RTAB_STRIDE) : nullptr);
;         SEAM(pb0);
.LBB0_1380:
	s_bitcmp1_b32 s83, 2
	s_cbranch_scc0 .Lseam5_go
	s_mov_b32 s99, 1
	s_mov_b64 s[0:1], s[78:79]
	s_lshl_b32 s2, s33, 9
	s_mul_i32 s3, s85, 0x4100
	s_lshl_b32 s48, s33, 3
	s_lshl_b32 s49, s83, 9
	s_lshl_b32 s50, s83, 3
	s_add_i32 s50, s50, s85
	s_lshl_b32 s88, s85, 6
	s_branch .Lconv_entry
